# router H-row loads hoisted 16 deep + P4 epilogue loads 16 deep + R2 rewrite
# speedup vs baseline: 1.0675x; 1.0315x over previous
.LBB0_778:
	s_lshl_b32 s20, s51, 8
	s_add_i32 s20, s20, s41
	v_readlane_b32 s52, v253, 2
	v_add_u32_e32 v228, s20, v146
	s_lshl_b32 s20, s12, 8
	s_or_b32 s20, s20, s42
	v_lshl_add_u32 v229, v1, 2, s20
	v_ashrrev_i32_e32 v240, 31, v228
	v_mov_b32_e32 v230, v228
	v_mov_b32_e32 v231, v240
	v_lshlrev_b64 v[230:231], 10, v[230:231]
	v_mov_b32_e32 v234, v229
	v_ashrrev_i32_e32 v235, 31, v229
	v_lshl_add_u64 v[230:231], v[230:231], 0, v[234:235]
	v_readlane_b32 s53, v253, 3
	s_lshl_b32 s20, s12, 2
	s_ashr_i32 s21, s20, 31
	v_lshl_add_u64 v[246:247], v[230:231], 2, s[52:53]
	v_lshl_add_u64 v[248:249], v[230:231], 1, s[84:85]
	v_mov_b32_e32 v250, v228
	v_mov_b32_e32 v251, v240
	v_lshlrev_b64 v[250:251], 6, v[250:251]
	v_lshl_add_u64 v[250:251], s[14:15], 0, v[250:251]
	v_lshl_add_u64 v[250:251], s[20:21], 2, v[250:251]
	s_lshl_b32 s12, s39, 2
	v_lshl_add_u64 v[250:251], v[250:251], 0, s[12:13]
	v_and_b32_e32 v241, 64, v151
	v_add_u32_e32 v241, 64, v241
	v_xor_b32_e32 v236, 16, v151
	v_cmp_lt_i32_e32 vcc, v236, v241
	s_nop 1
	v_cndmask_b32_e32 v236, v151, v236, vcc
	v_lshlrev_b32_e32 v236, 2, v236
	v_xor_b32_e32 v237, 32, v151
	v_cmp_lt_i32_e32 vcc, v237, v241
	s_nop 1
	v_cndmask_b32_e32 v237, v151, v237, vcc
	v_lshlrev_b32_e32 v237, 2, v237
	v_mov_b32_e32 v232, v246
	v_mov_b32_e32 v233, v247
	global_load_dwordx4 v[164:167], v[232:233], off
	global_load_dwordx4 v[168:171], v[232:233], off offset:64
	global_load_dwordx4 v[172:175], v[232:233], off offset:512
	global_load_dwordx4 v[176:179], v[232:233], off offset:576
	v_add_co_u32_e32 v232, vcc, 0x10000, v246
	s_nop 1
	v_addc_co_u32_e32 v233, vcc, 0, v247, vcc
	global_load_dwordx4 v[180:183], v[232:233], off
	global_load_dwordx4 v[184:187], v[232:233], off offset:64
	global_load_dwordx4 v[188:191], v[232:233], off offset:512
	global_load_dwordx4 v[192:195], v[232:233], off offset:576
	v_add_co_u32_e32 v232, vcc, 0x20000, v246
	s_nop 1
	v_addc_co_u32_e32 v233, vcc, 0, v247, vcc
	global_load_dwordx4 v[196:199], v[232:233], off
	global_load_dwordx4 v[200:203], v[232:233], off offset:64
	global_load_dwordx4 v[204:207], v[232:233], off offset:512
	global_load_dwordx4 v[208:211], v[232:233], off offset:576
	v_add_co_u32_e32 v232, vcc, 0x30000, v246
	s_nop 1
	v_addc_co_u32_e32 v233, vcc, 0, v247, vcc
	global_load_dwordx4 v[212:215], v[232:233], off
	global_load_dwordx4 v[216:219], v[232:233], off offset:64
	global_load_dwordx4 v[220:223], v[232:233], off offset:512
	global_load_dwordx4 v[224:227], v[232:233], off offset:576
	v_mov_b32_e32 v234, v248
	v_mov_b32_e32 v235, v249
	s_waitcnt vmcnt(15)
	v_pk_add_f32 v[166:167], v[128:129], v[166:167]
	v_pk_add_f32 v[164:165], v[126:127], v[164:165]
	v_cvt_pk_bf16_f32 v127, v166, v167
	v_cvt_pk_bf16_f32 v126, v164, v165
	global_store_dwordx2 v[234:235], v[126:127], off
	v_mul_f32_e32 v240, v165, v165
	v_mul_f32_e32 v241, v167, v167
	v_fmac_f32_e32 v240, v164, v164
	v_fmac_f32_e32 v241, v166, v166
	v_add_f32_e32 v242, v240, v241
	s_waitcnt vmcnt(15)
	v_pk_add_f32 v[170:171], v[124:125], v[170:171]
	v_pk_add_f32 v[168:169], v[122:123], v[168:169]
	v_cvt_pk_bf16_f32 v123, v170, v171
	v_cvt_pk_bf16_f32 v122, v168, v169
	global_store_dwordx2 v[234:235], v[122:123], off offset:32
	v_mul_f32_e32 v240, v169, v169
	v_mul_f32_e32 v241, v171, v171
	v_fmac_f32_e32 v240, v168, v168
	v_fmac_f32_e32 v241, v170, v170
	v_add_f32_e32 v240, v240, v241
	v_add_f32_e32 v242, v242, v240
	s_waitcnt vmcnt(15)
	v_pk_add_f32 v[174:175], v[120:121], v[174:175]
	v_pk_add_f32 v[172:173], v[118:119], v[172:173]
	v_cvt_pk_bf16_f32 v119, v174, v175
	v_cvt_pk_bf16_f32 v118, v172, v173
	global_store_dwordx2 v[234:235], v[118:119], off offset:256
	v_mul_f32_e32 v240, v173, v173
	v_mul_f32_e32 v241, v175, v175
	v_fmac_f32_e32 v240, v172, v172
	v_fmac_f32_e32 v241, v174, v174
	v_add_f32_e32 v240, v240, v241
	v_add_f32_e32 v242, v242, v240
	s_waitcnt vmcnt(15)
	v_pk_add_f32 v[178:179], v[116:117], v[178:179]
	v_pk_add_f32 v[176:177], v[114:115], v[176:177]
	v_cvt_pk_bf16_f32 v115, v178, v179
	v_cvt_pk_bf16_f32 v114, v176, v177
	global_store_dwordx2 v[234:235], v[114:115], off offset:288
	v_mul_f32_e32 v240, v177, v177
	v_mul_f32_e32 v241, v179, v179
	v_fmac_f32_e32 v240, v176, v176
	v_fmac_f32_e32 v241, v178, v178
	v_add_f32_e32 v240, v240, v241
	v_add_f32_e32 v242, v242, v240
	v_add_co_u32_e32 v232, vcc, 0x80000, v246
	s_nop 1
	v_addc_co_u32_e32 v233, vcc, 0, v247, vcc
	global_load_dwordx4 v[164:167], v[232:233], off
	global_load_dwordx4 v[168:171], v[232:233], off offset:64
	global_load_dwordx4 v[172:175], v[232:233], off offset:512
	global_load_dwordx4 v[176:179], v[232:233], off offset:576
	ds_bpermute_b32 v243, v236, v242
	v_mov_b32_e32 v238, v250
	v_mov_b32_e32 v239, v251
	s_waitcnt lgkmcnt(0)
	v_add_f32_e32 v242, v242, v243
	ds_bpermute_b32 v243, v237, v242
	v_cmp_eq_u32_e32 vcc, 0, v1
	s_waitcnt lgkmcnt(0)
	s_and_saveexec_b64 s[22:23], vcc
	v_add_f32_e32 v242, v242, v243
	global_store_dword v[238:239], v242, off
	s_or_b64 exec, exec, s[22:23]
	v_add_co_u32_e32 v234, vcc, 0x8000, v248
	s_nop 1
	v_addc_co_u32_e32 v235, vcc, 0, v249, vcc
	s_waitcnt vmcnt(20)
	v_pk_add_f32 v[182:183], v[112:113], v[182:183]
	v_pk_add_f32 v[180:181], v[110:111], v[180:181]
	v_cvt_pk_bf16_f32 v111, v182, v183
	v_cvt_pk_bf16_f32 v110, v180, v181
	global_store_dwordx2 v[234:235], v[110:111], off
	v_mul_f32_e32 v240, v181, v181
	v_mul_f32_e32 v241, v183, v183
	v_fmac_f32_e32 v240, v180, v180
	v_fmac_f32_e32 v241, v182, v182
	v_add_f32_e32 v242, v240, v241
	s_waitcnt vmcnt(20)
	v_pk_add_f32 v[186:187], v[108:109], v[186:187]
	v_pk_add_f32 v[184:185], v[106:107], v[184:185]
	v_cvt_pk_bf16_f32 v107, v186, v187
	v_cvt_pk_bf16_f32 v106, v184, v185
	global_store_dwordx2 v[234:235], v[106:107], off offset:32
	v_mul_f32_e32 v240, v185, v185
	v_mul_f32_e32 v241, v187, v187
	v_fmac_f32_e32 v240, v184, v184
	v_fmac_f32_e32 v241, v186, v186
	v_add_f32_e32 v240, v240, v241
	v_add_f32_e32 v242, v242, v240
	s_waitcnt vmcnt(20)
	v_pk_add_f32 v[190:191], v[104:105], v[190:191]
	v_pk_add_f32 v[188:189], v[102:103], v[188:189]
	v_cvt_pk_bf16_f32 v103, v190, v191
	v_cvt_pk_bf16_f32 v102, v188, v189
	global_store_dwordx2 v[234:235], v[102:103], off offset:256
	v_mul_f32_e32 v240, v189, v189
	v_mul_f32_e32 v241, v191, v191
	v_fmac_f32_e32 v240, v188, v188
	v_fmac_f32_e32 v241, v190, v190
	v_add_f32_e32 v240, v240, v241
	v_add_f32_e32 v242, v242, v240
	s_waitcnt vmcnt(20)
	v_pk_add_f32 v[194:195], v[100:101], v[194:195]
	v_pk_add_f32 v[192:193], v[98:99], v[192:193]
	v_cvt_pk_bf16_f32 v99, v194, v195
	v_cvt_pk_bf16_f32 v98, v192, v193
	global_store_dwordx2 v[234:235], v[98:99], off offset:288
	v_mul_f32_e32 v240, v193, v193
	v_mul_f32_e32 v241, v195, v195
	v_fmac_f32_e32 v240, v192, v192
	v_fmac_f32_e32 v241, v194, v194
	v_add_f32_e32 v240, v240, v241
	v_add_f32_e32 v242, v242, v240
	v_add_co_u32_e32 v232, vcc, 0x90000, v246
	s_nop 1
	v_addc_co_u32_e32 v233, vcc, 0, v247, vcc
	global_load_dwordx4 v[180:183], v[232:233], off
	global_load_dwordx4 v[184:187], v[232:233], off offset:64
	global_load_dwordx4 v[188:191], v[232:233], off offset:512
	global_load_dwordx4 v[192:195], v[232:233], off offset:576
	ds_bpermute_b32 v243, v236, v242
	v_add_co_u32_e32 v238, vcc, 0x400, v250
	s_nop 1
	v_addc_co_u32_e32 v239, vcc, 0, v251, vcc
	s_waitcnt lgkmcnt(0)
	v_add_f32_e32 v242, v242, v243
	ds_bpermute_b32 v243, v237, v242
	v_cmp_eq_u32_e32 vcc, 0, v1
	s_waitcnt lgkmcnt(0)
	s_and_saveexec_b64 s[22:23], vcc
	v_add_f32_e32 v242, v242, v243
	global_store_dword v[238:239], v242, off
	s_or_b64 exec, exec, s[22:23]
	v_add_co_u32_e32 v234, vcc, 0x10000, v248
	s_nop 1
	v_addc_co_u32_e32 v235, vcc, 0, v249, vcc
	s_waitcnt vmcnt(25)
	v_pk_add_f32 v[198:199], v[96:97], v[198:199]
	v_pk_add_f32 v[196:197], v[94:95], v[196:197]
	v_cvt_pk_bf16_f32 v95, v198, v199
	v_cvt_pk_bf16_f32 v94, v196, v197
	global_store_dwordx2 v[234:235], v[94:95], off
	v_mul_f32_e32 v240, v197, v197
	v_mul_f32_e32 v241, v199, v199
	v_fmac_f32_e32 v240, v196, v196
	v_fmac_f32_e32 v241, v198, v198
	v_add_f32_e32 v242, v240, v241
	s_waitcnt vmcnt(25)
	v_pk_add_f32 v[202:203], v[92:93], v[202:203]
	v_pk_add_f32 v[200:201], v[90:91], v[200:201]
	v_cvt_pk_bf16_f32 v91, v202, v203
	v_cvt_pk_bf16_f32 v90, v200, v201
	global_store_dwordx2 v[234:235], v[90:91], off offset:32
	v_mul_f32_e32 v240, v201, v201
	v_mul_f32_e32 v241, v203, v203
	v_fmac_f32_e32 v240, v200, v200
	v_fmac_f32_e32 v241, v202, v202
	v_add_f32_e32 v240, v240, v241
	v_add_f32_e32 v242, v242, v240
	s_waitcnt vmcnt(25)
	v_pk_add_f32 v[206:207], v[88:89], v[206:207]
	v_pk_add_f32 v[204:205], v[86:87], v[204:205]
	v_cvt_pk_bf16_f32 v87, v206, v207
	v_cvt_pk_bf16_f32 v86, v204, v205
	global_store_dwordx2 v[234:235], v[86:87], off offset:256
	v_mul_f32_e32 v240, v205, v205
	v_mul_f32_e32 v241, v207, v207
	v_fmac_f32_e32 v240, v204, v204
	v_fmac_f32_e32 v241, v206, v206
	v_add_f32_e32 v240, v240, v241
	v_add_f32_e32 v242, v242, v240
	s_waitcnt vmcnt(25)
	v_pk_add_f32 v[210:211], v[84:85], v[210:211]
	v_pk_add_f32 v[208:209], v[82:83], v[208:209]
	v_cvt_pk_bf16_f32 v83, v210, v211
	v_cvt_pk_bf16_f32 v82, v208, v209
	global_store_dwordx2 v[234:235], v[82:83], off offset:288
	v_mul_f32_e32 v240, v209, v209
	v_mul_f32_e32 v241, v211, v211
	v_fmac_f32_e32 v240, v208, v208
	v_fmac_f32_e32 v241, v210, v210
	v_add_f32_e32 v240, v240, v241
	v_add_f32_e32 v242, v242, v240
	v_add_co_u32_e32 v232, vcc, 0xa0000, v246
	s_nop 1
	v_addc_co_u32_e32 v233, vcc, 0, v247, vcc
	global_load_dwordx4 v[196:199], v[232:233], off
	global_load_dwordx4 v[200:203], v[232:233], off offset:64
	global_load_dwordx4 v[204:207], v[232:233], off offset:512
	global_load_dwordx4 v[208:211], v[232:233], off offset:576
	ds_bpermute_b32 v243, v236, v242
	v_add_co_u32_e32 v238, vcc, 0x800, v250
	s_nop 1
	v_addc_co_u32_e32 v239, vcc, 0, v251, vcc
	s_waitcnt lgkmcnt(0)
	v_add_f32_e32 v242, v242, v243
	ds_bpermute_b32 v243, v237, v242
	v_cmp_eq_u32_e32 vcc, 0, v1
	s_waitcnt lgkmcnt(0)
	s_and_saveexec_b64 s[22:23], vcc
	v_add_f32_e32 v242, v242, v243
	global_store_dword v[238:239], v242, off
	s_or_b64 exec, exec, s[22:23]
	v_add_co_u32_e32 v234, vcc, 0x18000, v248
	s_nop 1
	v_addc_co_u32_e32 v235, vcc, 0, v249, vcc
	s_waitcnt vmcnt(30)
	v_pk_add_f32 v[214:215], v[80:81], v[214:215]
	v_pk_add_f32 v[212:213], v[78:79], v[212:213]
	v_cvt_pk_bf16_f32 v79, v214, v215
	v_cvt_pk_bf16_f32 v78, v212, v213
	global_store_dwordx2 v[234:235], v[78:79], off
	v_mul_f32_e32 v240, v213, v213
	v_mul_f32_e32 v241, v215, v215
	v_fmac_f32_e32 v240, v212, v212
	v_fmac_f32_e32 v241, v214, v214
	v_add_f32_e32 v242, v240, v241
	s_waitcnt vmcnt(30)
	v_pk_add_f32 v[218:219], v[76:77], v[218:219]
	v_pk_add_f32 v[216:217], v[74:75], v[216:217]
	v_cvt_pk_bf16_f32 v75, v218, v219
	v_cvt_pk_bf16_f32 v74, v216, v217
	global_store_dwordx2 v[234:235], v[74:75], off offset:32
	v_mul_f32_e32 v240, v217, v217
	v_mul_f32_e32 v241, v219, v219
	v_fmac_f32_e32 v240, v216, v216
	v_fmac_f32_e32 v241, v218, v218
	v_add_f32_e32 v240, v240, v241
	v_add_f32_e32 v242, v242, v240
	s_waitcnt vmcnt(30)
	v_pk_add_f32 v[222:223], v[72:73], v[222:223]
	v_pk_add_f32 v[220:221], v[70:71], v[220:221]
	v_cvt_pk_bf16_f32 v71, v222, v223
	v_cvt_pk_bf16_f32 v70, v220, v221
	global_store_dwordx2 v[234:235], v[70:71], off offset:256
	v_mul_f32_e32 v240, v221, v221
	v_mul_f32_e32 v241, v223, v223
	v_fmac_f32_e32 v240, v220, v220
	v_fmac_f32_e32 v241, v222, v222
	v_add_f32_e32 v240, v240, v241
	v_add_f32_e32 v242, v242, v240
	s_waitcnt vmcnt(30)
	v_pk_add_f32 v[226:227], v[68:69], v[226:227]
	v_pk_add_f32 v[224:225], v[66:67], v[224:225]
	v_cvt_pk_bf16_f32 v67, v226, v227
	v_cvt_pk_bf16_f32 v66, v224, v225
	global_store_dwordx2 v[234:235], v[66:67], off offset:288
	v_mul_f32_e32 v240, v225, v225
	v_mul_f32_e32 v241, v227, v227
	v_fmac_f32_e32 v240, v224, v224
	v_fmac_f32_e32 v241, v226, v226
	v_add_f32_e32 v240, v240, v241
	v_add_f32_e32 v242, v242, v240
	v_add_co_u32_e32 v232, vcc, 0xb0000, v246
	s_nop 1
	v_addc_co_u32_e32 v233, vcc, 0, v247, vcc
	global_load_dwordx4 v[212:215], v[232:233], off
	global_load_dwordx4 v[216:219], v[232:233], off offset:64
	global_load_dwordx4 v[220:223], v[232:233], off offset:512
	global_load_dwordx4 v[224:227], v[232:233], off offset:576
	ds_bpermute_b32 v243, v236, v242
	v_add_co_u32_e32 v238, vcc, 0xc00, v250
	s_nop 1
	v_addc_co_u32_e32 v239, vcc, 0, v251, vcc
	s_waitcnt lgkmcnt(0)
	v_add_f32_e32 v242, v242, v243
	ds_bpermute_b32 v243, v237, v242
	v_cmp_eq_u32_e32 vcc, 0, v1
	s_waitcnt lgkmcnt(0)
	s_and_saveexec_b64 s[22:23], vcc
	v_add_f32_e32 v242, v242, v243
	global_store_dword v[238:239], v242, off
	s_or_b64 exec, exec, s[22:23]
	v_add_co_u32_e32 v234, vcc, 0x40000, v248
	s_nop 1
	v_addc_co_u32_e32 v235, vcc, 0, v249, vcc
	s_waitcnt vmcnt(31)
	v_pk_add_f32 v[166:167], v[64:65], v[166:167]
	v_pk_add_f32 v[164:165], v[62:63], v[164:165]
	v_cvt_pk_bf16_f32 v63, v166, v167
	v_cvt_pk_bf16_f32 v62, v164, v165
	global_store_dwordx2 v[234:235], v[62:63], off
	v_mul_f32_e32 v240, v165, v165
	v_mul_f32_e32 v241, v167, v167
	v_fmac_f32_e32 v240, v164, v164
	v_fmac_f32_e32 v241, v166, v166
	v_add_f32_e32 v242, v240, v241
	s_waitcnt vmcnt(31)
	v_pk_add_f32 v[170:171], v[60:61], v[170:171]
	v_pk_add_f32 v[168:169], v[58:59], v[168:169]
	v_cvt_pk_bf16_f32 v59, v170, v171
	v_cvt_pk_bf16_f32 v58, v168, v169
	global_store_dwordx2 v[234:235], v[58:59], off offset:32
	v_mul_f32_e32 v240, v169, v169
	v_mul_f32_e32 v241, v171, v171
	v_fmac_f32_e32 v240, v168, v168
	v_fmac_f32_e32 v241, v170, v170
	v_add_f32_e32 v240, v240, v241
	v_add_f32_e32 v242, v242, v240
	s_waitcnt vmcnt(31)
	v_pk_add_f32 v[174:175], v[56:57], v[174:175]
	v_pk_add_f32 v[172:173], v[54:55], v[172:173]
	v_cvt_pk_bf16_f32 v55, v174, v175
	v_cvt_pk_bf16_f32 v54, v172, v173
	global_store_dwordx2 v[234:235], v[54:55], off offset:256
	v_mul_f32_e32 v240, v173, v173
	v_mul_f32_e32 v241, v175, v175
	v_fmac_f32_e32 v240, v172, v172
	v_fmac_f32_e32 v241, v174, v174
	v_add_f32_e32 v240, v240, v241
	v_add_f32_e32 v242, v242, v240
	s_waitcnt vmcnt(31)
	v_pk_add_f32 v[178:179], v[52:53], v[178:179]
	v_pk_add_f32 v[176:177], v[50:51], v[176:177]
	v_cvt_pk_bf16_f32 v51, v178, v179
	v_cvt_pk_bf16_f32 v50, v176, v177
	global_store_dwordx2 v[234:235], v[50:51], off offset:288
	v_mul_f32_e32 v240, v177, v177
	v_mul_f32_e32 v241, v179, v179
	v_fmac_f32_e32 v240, v176, v176
	v_fmac_f32_e32 v241, v178, v178
	v_add_f32_e32 v240, v240, v241
	v_add_f32_e32 v242, v242, v240
	ds_bpermute_b32 v243, v236, v242
	v_add_co_u32_e32 v238, vcc, 0x2000, v250
	s_nop 1
	v_addc_co_u32_e32 v239, vcc, 0, v251, vcc
	s_waitcnt lgkmcnt(0)
	v_add_f32_e32 v242, v242, v243
	ds_bpermute_b32 v243, v237, v242
	v_cmp_eq_u32_e32 vcc, 0, v1
	s_waitcnt lgkmcnt(0)
	s_and_saveexec_b64 s[22:23], vcc
	v_add_f32_e32 v242, v242, v243
	global_store_dword v[238:239], v242, off
	s_or_b64 exec, exec, s[22:23]
	v_add_co_u32_e32 v234, vcc, 0x48000, v248
	s_nop 1
	v_addc_co_u32_e32 v235, vcc, 0, v249, vcc
	s_waitcnt vmcnt(27)
	v_pk_add_f32 v[182:183], v[48:49], v[182:183]
	v_pk_add_f32 v[180:181], v[46:47], v[180:181]
	v_cvt_pk_bf16_f32 v47, v182, v183
	v_cvt_pk_bf16_f32 v46, v180, v181
	global_store_dwordx2 v[234:235], v[46:47], off
	v_mul_f32_e32 v240, v181, v181
	v_mul_f32_e32 v241, v183, v183
	v_fmac_f32_e32 v240, v180, v180
	v_fmac_f32_e32 v241, v182, v182
	v_add_f32_e32 v242, v240, v241
	s_waitcnt vmcnt(27)
	v_pk_add_f32 v[186:187], v[44:45], v[186:187]
	v_pk_add_f32 v[184:185], v[42:43], v[184:185]
	v_cvt_pk_bf16_f32 v43, v186, v187
	v_cvt_pk_bf16_f32 v42, v184, v185
	global_store_dwordx2 v[234:235], v[42:43], off offset:32
	v_mul_f32_e32 v240, v185, v185
	v_mul_f32_e32 v241, v187, v187
	v_fmac_f32_e32 v240, v184, v184
	v_fmac_f32_e32 v241, v186, v186
	v_add_f32_e32 v240, v240, v241
	v_add_f32_e32 v242, v242, v240
	s_waitcnt vmcnt(27)
	v_pk_add_f32 v[190:191], v[40:41], v[190:191]
	v_pk_add_f32 v[188:189], v[38:39], v[188:189]
	v_cvt_pk_bf16_f32 v39, v190, v191
	v_cvt_pk_bf16_f32 v38, v188, v189
	global_store_dwordx2 v[234:235], v[38:39], off offset:256
	v_mul_f32_e32 v240, v189, v189
	v_mul_f32_e32 v241, v191, v191
	v_fmac_f32_e32 v240, v188, v188
	v_fmac_f32_e32 v241, v190, v190
	v_add_f32_e32 v240, v240, v241
	v_add_f32_e32 v242, v242, v240
	s_waitcnt vmcnt(27)
	v_pk_add_f32 v[194:195], v[36:37], v[194:195]
	v_pk_add_f32 v[192:193], v[34:35], v[192:193]
	v_cvt_pk_bf16_f32 v35, v194, v195
	v_cvt_pk_bf16_f32 v34, v192, v193
	global_store_dwordx2 v[234:235], v[34:35], off offset:288
	v_mul_f32_e32 v240, v193, v193
	v_mul_f32_e32 v241, v195, v195
	v_fmac_f32_e32 v240, v192, v192
	v_fmac_f32_e32 v241, v194, v194
	v_add_f32_e32 v240, v240, v241
	v_add_f32_e32 v242, v242, v240
	ds_bpermute_b32 v243, v236, v242
	v_add_co_u32_e32 v238, vcc, 0x2400, v250
	s_nop 1
	v_addc_co_u32_e32 v239, vcc, 0, v251, vcc
	s_waitcnt lgkmcnt(0)
	v_add_f32_e32 v242, v242, v243
	ds_bpermute_b32 v243, v237, v242
	v_cmp_eq_u32_e32 vcc, 0, v1
	s_waitcnt lgkmcnt(0)
	s_and_saveexec_b64 s[22:23], vcc
	v_add_f32_e32 v242, v242, v243
	global_store_dword v[238:239], v242, off
	s_or_b64 exec, exec, s[22:23]
	v_add_co_u32_e32 v234, vcc, 0x50000, v248
	s_nop 1
	v_addc_co_u32_e32 v235, vcc, 0, v249, vcc
	s_waitcnt vmcnt(23)
	v_pk_add_f32 v[198:199], v[32:33], v[198:199]
	v_pk_add_f32 v[196:197], v[30:31], v[196:197]
	v_cvt_pk_bf16_f32 v31, v198, v199
	v_cvt_pk_bf16_f32 v30, v196, v197
	global_store_dwordx2 v[234:235], v[30:31], off
	v_mul_f32_e32 v240, v197, v197
	v_mul_f32_e32 v241, v199, v199
	v_fmac_f32_e32 v240, v196, v196
	v_fmac_f32_e32 v241, v198, v198
	v_add_f32_e32 v242, v240, v241
	s_waitcnt vmcnt(23)
	v_pk_add_f32 v[202:203], v[28:29], v[202:203]
	v_pk_add_f32 v[200:201], v[26:27], v[200:201]
	v_cvt_pk_bf16_f32 v27, v202, v203
	v_cvt_pk_bf16_f32 v26, v200, v201
	global_store_dwordx2 v[234:235], v[26:27], off offset:32
	v_mul_f32_e32 v240, v201, v201
	v_mul_f32_e32 v241, v203, v203
	v_fmac_f32_e32 v240, v200, v200
	v_fmac_f32_e32 v241, v202, v202
	v_add_f32_e32 v240, v240, v241
	v_add_f32_e32 v242, v242, v240
	s_waitcnt vmcnt(23)
	v_pk_add_f32 v[206:207], v[24:25], v[206:207]
	v_pk_add_f32 v[204:205], v[22:23], v[204:205]
	v_cvt_pk_bf16_f32 v23, v206, v207
	v_cvt_pk_bf16_f32 v22, v204, v205
	global_store_dwordx2 v[234:235], v[22:23], off offset:256
	v_mul_f32_e32 v240, v205, v205
	v_mul_f32_e32 v241, v207, v207
	v_fmac_f32_e32 v240, v204, v204
	v_fmac_f32_e32 v241, v206, v206
	v_add_f32_e32 v240, v240, v241
	v_add_f32_e32 v242, v242, v240
	s_waitcnt vmcnt(23)
	v_pk_add_f32 v[210:211], v[20:21], v[210:211]
	v_pk_add_f32 v[208:209], v[18:19], v[208:209]
	v_cvt_pk_bf16_f32 v19, v210, v211
	v_cvt_pk_bf16_f32 v18, v208, v209
	global_store_dwordx2 v[234:235], v[18:19], off offset:288
	v_mul_f32_e32 v240, v209, v209
	v_mul_f32_e32 v241, v211, v211
	v_fmac_f32_e32 v240, v208, v208
	v_fmac_f32_e32 v241, v210, v210
	v_add_f32_e32 v240, v240, v241
	v_add_f32_e32 v242, v242, v240
	ds_bpermute_b32 v243, v236, v242
	v_add_co_u32_e32 v238, vcc, 0x2800, v250
	s_nop 1
	v_addc_co_u32_e32 v239, vcc, 0, v251, vcc
	s_waitcnt lgkmcnt(0)
	v_add_f32_e32 v242, v242, v243
	ds_bpermute_b32 v243, v237, v242
	v_cmp_eq_u32_e32 vcc, 0, v1
	s_waitcnt lgkmcnt(0)
	s_and_saveexec_b64 s[22:23], vcc
	v_add_f32_e32 v242, v242, v243
	global_store_dword v[238:239], v242, off
	s_or_b64 exec, exec, s[22:23]
	v_add_co_u32_e32 v234, vcc, 0x58000, v248
	s_nop 1
	v_addc_co_u32_e32 v235, vcc, 0, v249, vcc
	s_waitcnt vmcnt(19)
	v_pk_add_f32 v[214:215], v[16:17], v[214:215]
	v_pk_add_f32 v[212:213], v[14:15], v[212:213]
	v_cvt_pk_bf16_f32 v15, v214, v215
	v_cvt_pk_bf16_f32 v14, v212, v213
	global_store_dwordx2 v[234:235], v[14:15], off
	v_mul_f32_e32 v240, v213, v213
	v_mul_f32_e32 v241, v215, v215
	v_fmac_f32_e32 v240, v212, v212
	v_fmac_f32_e32 v241, v214, v214
	v_add_f32_e32 v242, v240, v241
	s_waitcnt vmcnt(19)
	v_pk_add_f32 v[218:219], v[12:13], v[218:219]
	v_pk_add_f32 v[216:217], v[10:11], v[216:217]
	v_cvt_pk_bf16_f32 v11, v218, v219
	v_cvt_pk_bf16_f32 v10, v216, v217
	global_store_dwordx2 v[234:235], v[10:11], off offset:32
	v_mul_f32_e32 v240, v217, v217
	v_mul_f32_e32 v241, v219, v219
	v_fmac_f32_e32 v240, v216, v216
	v_fmac_f32_e32 v241, v218, v218
	v_add_f32_e32 v240, v240, v241
	v_add_f32_e32 v242, v242, v240
	s_waitcnt vmcnt(19)
	v_pk_add_f32 v[222:223], v[8:9], v[222:223]
	v_pk_add_f32 v[220:221], v[6:7], v[220:221]
	v_cvt_pk_bf16_f32 v7, v222, v223
	v_cvt_pk_bf16_f32 v6, v220, v221
	global_store_dwordx2 v[234:235], v[6:7], off offset:256
	v_mul_f32_e32 v240, v221, v221
	v_mul_f32_e32 v241, v223, v223
	v_fmac_f32_e32 v240, v220, v220
	v_fmac_f32_e32 v241, v222, v222
	v_add_f32_e32 v240, v240, v241
	v_add_f32_e32 v242, v242, v240
	s_waitcnt vmcnt(19)
	v_pk_add_f32 v[226:227], v[4:5], v[226:227]
	v_pk_add_f32 v[224:225], v[2:3], v[224:225]
	v_cvt_pk_bf16_f32 v3, v226, v227
	v_cvt_pk_bf16_f32 v2, v224, v225
	global_store_dwordx2 v[234:235], v[2:3], off offset:288
	v_mul_f32_e32 v240, v225, v225
	v_mul_f32_e32 v241, v227, v227
	v_fmac_f32_e32 v240, v224, v224
	v_fmac_f32_e32 v241, v226, v226
	v_add_f32_e32 v240, v240, v241
	v_add_f32_e32 v242, v242, v240
	ds_bpermute_b32 v243, v236, v242
	v_add_co_u32_e32 v238, vcc, 0x2c00, v250
	s_nop 1
	v_addc_co_u32_e32 v239, vcc, 0, v251, vcc
	s_waitcnt lgkmcnt(0)
	v_add_f32_e32 v242, v242, v243
	ds_bpermute_b32 v243, v237, v242
	v_cmp_eq_u32_e32 vcc, 0, v1
	s_waitcnt lgkmcnt(0)
	s_and_saveexec_b64 s[22:23], vcc
	v_add_f32_e32 v242, v242, v243
	global_store_dword v[238:239], v242, off
	s_branch .LBB0_764

.LBB0_1043:
	v_add_u32_e32 v18, s8, v22
	v_mov_b32_e32 v116, v18
	v_ashrrev_i32_e32 v117, 31, v116
	v_lshlrev_b64 v[116:117], 11, v[116:117]
	v_lshl_add_u64 v[116:117], v[24:25], 0, v[116:117]
	v_add_u32_e32 v118, 1, v18
	v_ashrrev_i32_e32 v119, 31, v118
	v_lshlrev_b64 v[118:119], 11, v[118:119]
	v_lshl_add_u64 v[118:119], v[24:25], 0, v[118:119]
	v_add_u32_e32 v120, 2, v18
	v_ashrrev_i32_e32 v121, 31, v120
	v_lshlrev_b64 v[120:121], 11, v[120:121]
	v_lshl_add_u64 v[120:121], v[24:25], 0, v[120:121]
	v_add_u32_e32 v122, 3, v18
	v_ashrrev_i32_e32 v123, 31, v122
	v_lshlrev_b64 v[122:123], 11, v[122:123]
	v_lshl_add_u64 v[122:123], v[24:25], 0, v[122:123]
	global_load_dwordx2 v[84:85], v[116:117], off
	global_load_dwordx2 v[86:87], v[116:117], off offset:512
	global_load_dwordx2 v[88:89], v[116:117], off offset:1024
	global_load_dwordx2 v[90:91], v[116:117], off offset:1536
	global_load_dwordx2 v[92:93], v[118:119], off
	global_load_dwordx2 v[94:95], v[118:119], off offset:512
	global_load_dwordx2 v[96:97], v[118:119], off offset:1024
	global_load_dwordx2 v[98:99], v[118:119], off offset:1536
	global_load_dwordx2 v[100:101], v[120:121], off
	global_load_dwordx2 v[102:103], v[120:121], off offset:512
	global_load_dwordx2 v[104:105], v[120:121], off offset:1024
	global_load_dwordx2 v[106:107], v[120:121], off offset:1536
	global_load_dwordx2 v[108:109], v[122:123], off
	global_load_dwordx2 v[110:111], v[122:123], off offset:512
	global_load_dwordx2 v[112:113], v[122:123], off offset:1024
	global_load_dwordx2 v[114:115], v[122:123], off offset:1536
	v_ashrrev_i32_e32 v19, 31, v18
	s_waitcnt lgkmcnt(0)
	v_lshlrev_b64 v[62:63], 11, v[18:19]
	v_lshl_add_u64 v[62:63], v[24:25], 0, v[62:63]
	ds_bpermute_b32 v35, v34, v33
	v_add_u32_e32 v20, 1, v18
	v_add_u32_e32 v36, 2, v18
	v_ashrrev_i32_e32 v21, 31, v20
	v_ashrrev_i32_e32 v37, 31, v36
	v_lshlrev_b64 v[64:65], 10, v[20:21]
	v_lshlrev_b64 v[20:21], 11, v[20:21]
	v_lshlrev_b64 v[66:67], 10, v[36:37]
	v_lshlrev_b64 v[60:61], 10, v[18:19]
	v_lshl_add_u64 v[70:71], v[24:25], 0, v[20:21]
	v_lshl_add_u64 v[20:21], v[26:27], 0, v[66:67]
	s_waitcnt lgkmcnt(0)
	v_mul_f32_e32 v19, 0x41800000, v35
	v_mov_b32_e32 v59, 0
	v_lshl_add_u64 v[60:61], v[26:27], 0, v[60:61]
	v_mov_b32_e32 v72, 0
	v_mov_b32_e32 v73, 0
	v_mov_b32_e32 v74, 0
	ds_bpermute_b32 v75, v34, v33 offset:4
	v_mov_b32_e32 v76, 0
	v_lshl_add_u64 v[64:65], v[26:27], 0, v[64:65]
	v_mov_b32_e32 v77, 0
	v_mov_b32_e32 v78, 0
	s_waitcnt lgkmcnt(0)
	v_mul_f32_e32 v35, 0x41800000, v75
	v_mov_b32_e32 v79, 0
	v_lshlrev_b64 v[36:37], 11, v[36:37]
	v_lshl_add_u64 v[36:37], v[24:25], 0, v[36:37]
	ds_bpermute_b32 v80, v34, v33 offset:8
	v_mov_b32_e32 v81, 0
	v_mov_b32_e32 v82, 0
	v_add_u32_e32 v18, 3, v18
	s_add_i32 s8, s8, 4
	s_waitcnt lgkmcnt(0)
	v_mul_f32_e32 v75, 0x41800000, v80
	s_cmp_eq_u32 s8, 8
	s_waitcnt vmcnt(15)
	v_mov_b32_e32 v68, v84
	v_mov_b32_e32 v69, v85
	v_lshlrev_b32_e32 v66, 16, v68
	v_and_b32_e32 v67, 0xffff0000, v68
	v_mul_f32_e32 v66, v19, v66
	v_mul_f32_e32 v67, v19, v67
	v_mul_f32_e32 v66, v2, v66
	v_mul_f32_e32 v67, v3, v67
	v_med3_f32 v66, v66, s15, v58
	v_med3_f32 v67, v67, s15, v58
	v_lshlrev_b32_e32 v68, 16, v69
	v_and_b32_e32 v69, 0xffff0000, v69
	v_cvt_pk_fp8_f32 v59, v66, v67
	v_mul_f32_e32 v68, v19, v68
	v_mul_f32_e32 v69, v19, v69
	v_mul_f32_e32 v68, v4, v68
	v_mul_f32_e32 v69, v5, v69
	v_med3_f32 v68, v68, s15, v58
	v_med3_f32 v69, v69, s15, v58
	v_cvt_pk_fp8_f32 v59, v68, v69 op_sel:[0,0,1]
	global_store_dword v[60:61], v59, off
	s_waitcnt vmcnt(15)
	v_mov_b32_e32 v66, v86
	v_mov_b32_e32 v67, v87
	v_lshlrev_b32_e32 v59, 16, v66
	v_and_b32_e32 v66, 0xffff0000, v66
	v_mul_f32_e32 v59, v19, v59
	v_mul_f32_e32 v66, v19, v66
	v_mul_f32_e32 v59, v6, v59
	v_mul_f32_e32 v66, v7, v66
	v_med3_f32 v59, v59, s15, v58
	v_med3_f32 v66, v66, s15, v58
	v_lshlrev_b32_e32 v68, 16, v67
	v_and_b32_e32 v67, 0xffff0000, v67
	v_cvt_pk_fp8_f32 v72, v59, v66
	v_mul_f32_e32 v68, v19, v68
	v_mul_f32_e32 v67, v19, v67
	v_mul_f32_e32 v68, v8, v68
	v_mul_f32_e32 v67, v9, v67
	v_med3_f32 v68, v68, s15, v58
	v_med3_f32 v67, v67, s15, v58
	v_cvt_pk_fp8_f32 v72, v68, v67 op_sel:[0,0,1]
	global_store_dword v[60:61], v72, off offset:256
	s_waitcnt vmcnt(15)
	v_mov_b32_e32 v66, v88
	v_mov_b32_e32 v67, v89
	v_lshlrev_b32_e32 v59, 16, v66
	v_and_b32_e32 v66, 0xffff0000, v66
	v_mul_f32_e32 v59, v19, v59
	v_mul_f32_e32 v66, v19, v66
	v_mul_f32_e32 v59, v10, v59
	v_mul_f32_e32 v66, v11, v66
	v_med3_f32 v59, v59, s15, v58
	v_med3_f32 v66, v66, s15, v58
	v_lshlrev_b32_e32 v68, 16, v67
	v_and_b32_e32 v67, 0xffff0000, v67
	v_cvt_pk_fp8_f32 v73, v59, v66
	v_mul_f32_e32 v68, v19, v68
	v_mul_f32_e32 v67, v19, v67
	v_mul_f32_e32 v68, v12, v68
	v_mul_f32_e32 v67, v13, v67
	v_med3_f32 v68, v68, s15, v58
	v_med3_f32 v67, v67, s15, v58
	v_cvt_pk_fp8_f32 v73, v68, v67 op_sel:[0,0,1]
	global_store_dword v[60:61], v73, off offset:512
	s_waitcnt vmcnt(15)
	v_mov_b32_e32 v62, v90
	v_mov_b32_e32 v63, v91
	v_lshlrev_b32_e32 v59, 16, v62
	v_and_b32_e32 v62, 0xffff0000, v62
	v_mul_f32_e32 v59, v19, v59
	v_mul_f32_e32 v62, v19, v62
	v_mul_f32_e32 v59, v14, v59
	v_mul_f32_e32 v62, v15, v62
	v_med3_f32 v59, v59, s15, v58
	v_med3_f32 v62, v62, s15, v58
	v_lshlrev_b32_e32 v66, 16, v63
	v_and_b32_e32 v63, 0xffff0000, v63
	v_cvt_pk_fp8_f32 v74, v59, v62
	v_mul_f32_e32 v66, v19, v66
	v_mul_f32_e32 v19, v19, v63
	v_mul_f32_e32 v63, v16, v66
	v_mul_f32_e32 v19, v17, v19
	v_med3_f32 v63, v63, s15, v58
	v_med3_f32 v19, v19, s15, v58
	v_cvt_pk_fp8_f32 v74, v63, v19 op_sel:[0,0,1]
	global_store_dword v[60:61], v74, off offset:768
	s_waitcnt vmcnt(15)
	v_mov_b32_e32 v60, v92
	v_mov_b32_e32 v61, v93
	v_lshlrev_b32_e32 v19, 16, v60
	v_and_b32_e32 v59, 0xffff0000, v60
	v_mul_f32_e32 v19, v35, v19
	v_mul_f32_e32 v59, v35, v59
	v_mul_f32_e32 v19, v2, v19
	v_mul_f32_e32 v59, v3, v59
	v_med3_f32 v19, v19, s15, v58
	v_med3_f32 v59, v59, s15, v58
	v_lshlrev_b32_e32 v60, 16, v61
	v_and_b32_e32 v61, 0xffff0000, v61
	v_cvt_pk_fp8_f32 v76, v19, v59
	v_mul_f32_e32 v60, v35, v60
	v_mul_f32_e32 v61, v35, v61
	v_mul_f32_e32 v60, v4, v60
	v_mul_f32_e32 v61, v5, v61
	v_med3_f32 v60, v60, s15, v58
	v_med3_f32 v61, v61, s15, v58
	v_cvt_pk_fp8_f32 v76, v60, v61 op_sel:[0,0,1]
	global_store_dword v[64:65], v76, off
	s_waitcnt vmcnt(15)
	v_mov_b32_e32 v60, v94
	v_mov_b32_e32 v61, v95
	v_lshlrev_b32_e32 v19, 16, v60
	v_and_b32_e32 v59, 0xffff0000, v60
	v_mul_f32_e32 v19, v35, v19
	v_mul_f32_e32 v59, v35, v59
	v_mul_f32_e32 v19, v6, v19
	v_mul_f32_e32 v59, v7, v59
	v_med3_f32 v19, v19, s15, v58
	v_med3_f32 v59, v59, s15, v58
	v_lshlrev_b32_e32 v60, 16, v61
	v_and_b32_e32 v61, 0xffff0000, v61
	v_cvt_pk_fp8_f32 v77, v19, v59
	v_mul_f32_e32 v60, v35, v60
	v_mul_f32_e32 v61, v35, v61
	v_mul_f32_e32 v60, v8, v60
	v_mul_f32_e32 v61, v9, v61
	v_med3_f32 v60, v60, s15, v58
	v_med3_f32 v61, v61, s15, v58
	v_cvt_pk_fp8_f32 v77, v60, v61 op_sel:[0,0,1]
	global_store_dword v[64:65], v77, off offset:256
	s_waitcnt vmcnt(15)
	v_mov_b32_e32 v60, v96
	v_mov_b32_e32 v61, v97
	v_lshlrev_b32_e32 v19, 16, v60
	v_and_b32_e32 v59, 0xffff0000, v60
	v_mul_f32_e32 v19, v35, v19
	v_mul_f32_e32 v59, v35, v59
	v_mul_f32_e32 v19, v10, v19
	v_mul_f32_e32 v59, v11, v59
	v_med3_f32 v19, v19, s15, v58
	v_med3_f32 v59, v59, s15, v58
	v_lshlrev_b32_e32 v60, 16, v61
	v_and_b32_e32 v61, 0xffff0000, v61
	v_cvt_pk_fp8_f32 v78, v19, v59
	v_mul_f32_e32 v60, v35, v60
	v_mul_f32_e32 v61, v35, v61
	v_mul_f32_e32 v60, v12, v60
	v_mul_f32_e32 v61, v13, v61
	v_med3_f32 v60, v60, s15, v58
	v_med3_f32 v61, v61, s15, v58
	v_cvt_pk_fp8_f32 v78, v60, v61 op_sel:[0,0,1]
	global_store_dword v[64:65], v78, off offset:512
	s_waitcnt vmcnt(15)
	v_mov_b32_e32 v60, v98
	v_mov_b32_e32 v61, v99
	v_lshlrev_b32_e32 v19, 16, v60
	v_and_b32_e32 v59, 0xffff0000, v60
	v_mul_f32_e32 v19, v35, v19
	v_mul_f32_e32 v59, v35, v59
	v_mul_f32_e32 v19, v14, v19
	v_mul_f32_e32 v59, v15, v59
	v_med3_f32 v19, v19, s15, v58
	v_med3_f32 v59, v59, s15, v58
	v_lshlrev_b32_e32 v60, 16, v61
	v_and_b32_e32 v61, 0xffff0000, v61
	v_cvt_pk_fp8_f32 v79, v19, v59
	v_mul_f32_e32 v60, v35, v60
	v_mul_f32_e32 v35, v35, v61
	v_mul_f32_e32 v60, v16, v60
	v_mul_f32_e32 v35, v17, v35
	v_med3_f32 v60, v60, s15, v58
	v_med3_f32 v35, v35, s15, v58
	v_cvt_pk_fp8_f32 v79, v60, v35 op_sel:[0,0,1]
	global_store_dword v[64:65], v79, off offset:768
	s_waitcnt vmcnt(15)
	v_mov_b32_e32 v60, v100
	v_mov_b32_e32 v61, v101
	v_lshlrev_b32_e32 v19, 16, v60
	v_and_b32_e32 v35, 0xffff0000, v60
	v_mul_f32_e32 v19, v75, v19
	v_mul_f32_e32 v35, v75, v35
	v_mul_f32_e32 v19, v2, v19
	v_mul_f32_e32 v35, v3, v35
	v_med3_f32 v19, v19, s15, v58
	v_med3_f32 v35, v35, s15, v58
	v_lshlrev_b32_e32 v59, 16, v61
	v_and_b32_e32 v60, 0xffff0000, v61
	v_cvt_pk_fp8_f32 v81, v19, v35
	v_mul_f32_e32 v59, v75, v59
	v_mul_f32_e32 v60, v75, v60
	v_mul_f32_e32 v59, v4, v59
	v_mul_f32_e32 v60, v5, v60
	v_med3_f32 v59, v59, s15, v58
	v_med3_f32 v60, v60, s15, v58
	v_cvt_pk_fp8_f32 v81, v59, v60 op_sel:[0,0,1]
	global_store_dword v[20:21], v81, off
	s_waitcnt vmcnt(15)
	v_mov_b32_e32 v60, v102
	v_mov_b32_e32 v61, v103
	v_lshlrev_b32_e32 v19, 16, v60
	v_and_b32_e32 v35, 0xffff0000, v60
	v_mul_f32_e32 v19, v75, v19
	v_mul_f32_e32 v35, v75, v35
	v_mul_f32_e32 v19, v6, v19
	v_mul_f32_e32 v35, v7, v35
	v_med3_f32 v19, v19, s15, v58
	v_med3_f32 v35, v35, s15, v58
	v_lshlrev_b32_e32 v59, 16, v61
	v_and_b32_e32 v60, 0xffff0000, v61
	v_cvt_pk_fp8_f32 v82, v19, v35
	v_mul_f32_e32 v59, v75, v59
	v_mul_f32_e32 v60, v75, v60
	v_mul_f32_e32 v59, v8, v59
	v_mul_f32_e32 v60, v9, v60
	v_med3_f32 v59, v59, s15, v58
	v_med3_f32 v60, v60, s15, v58
	v_cvt_pk_fp8_f32 v82, v59, v60 op_sel:[0,0,1]
	v_mov_b32_e32 v19, 0
	global_store_dword v[20:21], v82, off offset:256
	s_waitcnt vmcnt(15)
	v_mov_b32_e32 v60, v104
	v_mov_b32_e32 v61, v105
	v_lshlrev_b32_e32 v35, 16, v60
	v_and_b32_e32 v59, 0xffff0000, v60
	v_mul_f32_e32 v35, v75, v35
	v_mul_f32_e32 v59, v75, v59
	v_mul_f32_e32 v35, v10, v35
	v_mul_f32_e32 v59, v11, v59
	v_med3_f32 v35, v35, s15, v58
	v_med3_f32 v59, v59, s15, v58
	v_lshlrev_b32_e32 v60, 16, v61
	v_and_b32_e32 v61, 0xffff0000, v61
	v_cvt_pk_fp8_f32 v19, v35, v59
	v_mul_f32_e32 v60, v75, v60
	v_mul_f32_e32 v61, v75, v61
	v_mul_f32_e32 v60, v12, v60
	v_mul_f32_e32 v61, v13, v61
	v_med3_f32 v60, v60, s15, v58
	v_med3_f32 v61, v61, s15, v58
	v_cvt_pk_fp8_f32 v19, v60, v61 op_sel:[0,0,1]
	v_mov_b32_e32 v35, 0
	global_store_dword v[20:21], v19, off offset:512
	v_ashrrev_i32_e32 v19, 31, v18
	v_lshlrev_b64 v[60:61], 11, v[18:19]
	v_lshl_add_u64 v[60:61], v[24:25], 0, v[60:61]
	v_lshlrev_b64 v[18:19], 10, v[18:19]
	v_lshl_add_u64 v[18:19], v[26:27], 0, v[18:19]
	s_waitcnt vmcnt(15)
	v_mov_b32_e32 v36, v106
	v_mov_b32_e32 v37, v107
	v_lshlrev_b32_e32 v59, 16, v36
	v_and_b32_e32 v36, 0xffff0000, v36
	v_mul_f32_e32 v59, v75, v59
	v_mul_f32_e32 v36, v75, v36
	v_mul_f32_e32 v59, v14, v59
	v_mul_f32_e32 v36, v15, v36
	v_med3_f32 v59, v59, s15, v58
	v_med3_f32 v36, v36, s15, v58
	v_lshlrev_b32_e32 v62, 16, v37
	v_and_b32_e32 v37, 0xffff0000, v37
	v_cvt_pk_fp8_f32 v35, v59, v36
	v_mul_f32_e32 v62, v75, v62
	v_mul_f32_e32 v37, v75, v37
	v_mul_f32_e32 v62, v16, v62
	v_mul_f32_e32 v37, v17, v37
	v_med3_f32 v62, v62, s15, v58
	v_med3_f32 v37, v37, s15, v58
	v_cvt_pk_fp8_f32 v35, v62, v37 op_sel:[0,0,1]
	v_mov_b32_e32 v36, 0
	global_store_dword v[20:21], v35, off offset:768
	ds_bpermute_b32 v35, v34, v33 offset:12
	v_add_u32_e32 v34, 16, v34
	s_waitcnt lgkmcnt(0)
	v_mul_f32_e32 v35, 0x41800000, v35
	s_waitcnt vmcnt(15)
	v_mov_b32_e32 v20, v108
	v_mov_b32_e32 v21, v109
	v_lshlrev_b32_e32 v37, 16, v20
	v_and_b32_e32 v20, 0xffff0000, v20
	v_mul_f32_e32 v37, v35, v37
	v_mul_f32_e32 v20, v35, v20
	v_mul_f32_e32 v37, v2, v37
	v_mul_f32_e32 v20, v3, v20
	v_med3_f32 v37, v37, s15, v58
	v_med3_f32 v20, v20, s15, v58
	v_lshlrev_b32_e32 v59, 16, v21
	v_and_b32_e32 v21, 0xffff0000, v21
	v_cvt_pk_fp8_f32 v36, v37, v20
	v_mul_f32_e32 v59, v35, v59
	v_mul_f32_e32 v21, v35, v21
	v_mul_f32_e32 v59, v4, v59
	v_mul_f32_e32 v21, v5, v21
	v_med3_f32 v59, v59, s15, v58
	v_med3_f32 v21, v21, s15, v58
	v_cvt_pk_fp8_f32 v36, v59, v21 op_sel:[0,0,1]
	global_store_dword v[18:19], v36, off
	v_mov_b32_e32 v36, 0
	s_waitcnt vmcnt(15)
	v_mov_b32_e32 v20, v110
	v_mov_b32_e32 v21, v111
	v_lshlrev_b32_e32 v37, 16, v20
	v_and_b32_e32 v20, 0xffff0000, v20
	v_mul_f32_e32 v37, v35, v37
	v_mul_f32_e32 v20, v35, v20
	v_mul_f32_e32 v37, v6, v37
	v_mul_f32_e32 v20, v7, v20
	v_med3_f32 v37, v37, s15, v58
	v_med3_f32 v20, v20, s15, v58
	v_lshlrev_b32_e32 v59, 16, v21
	v_and_b32_e32 v21, 0xffff0000, v21
	v_cvt_pk_fp8_f32 v36, v37, v20
	v_mul_f32_e32 v59, v35, v59
	v_mul_f32_e32 v21, v35, v21
	v_mul_f32_e32 v59, v8, v59
	v_mul_f32_e32 v21, v9, v21
	v_med3_f32 v59, v59, s15, v58
	v_med3_f32 v21, v21, s15, v58
	v_cvt_pk_fp8_f32 v36, v59, v21 op_sel:[0,0,1]
	global_store_dword v[18:19], v36, off offset:256
	v_mov_b32_e32 v36, 0
	s_waitcnt vmcnt(15)
	v_mov_b32_e32 v20, v112
	v_mov_b32_e32 v21, v113
	v_lshlrev_b32_e32 v37, 16, v20
	v_and_b32_e32 v20, 0xffff0000, v20
	v_mul_f32_e32 v37, v35, v37
	v_mul_f32_e32 v20, v35, v20
	v_mul_f32_e32 v37, v10, v37
	v_mul_f32_e32 v20, v11, v20
	v_med3_f32 v37, v37, s15, v58
	v_med3_f32 v20, v20, s15, v58
	v_lshlrev_b32_e32 v59, 16, v21
	v_and_b32_e32 v21, 0xffff0000, v21
	v_cvt_pk_fp8_f32 v36, v37, v20
	v_mul_f32_e32 v59, v35, v59
	v_mul_f32_e32 v21, v35, v21
	v_mul_f32_e32 v59, v12, v59
	v_mul_f32_e32 v21, v13, v21
	v_med3_f32 v59, v59, s15, v58
	v_med3_f32 v21, v21, s15, v58
	v_cvt_pk_fp8_f32 v36, v59, v21 op_sel:[0,0,1]
	global_store_dword v[18:19], v36, off offset:512
	v_mov_b32_e32 v36, 0
	s_waitcnt vmcnt(15)
	v_mov_b32_e32 v20, v114
	v_mov_b32_e32 v21, v115
	v_lshlrev_b32_e32 v37, 16, v20
	v_and_b32_e32 v20, 0xffff0000, v20
	v_lshlrev_b32_e32 v59, 16, v21
	v_and_b32_e32 v21, 0xffff0000, v21
	v_mul_f32_e32 v37, v35, v37
	v_mul_f32_e32 v20, v35, v20
	v_mul_f32_e32 v59, v35, v59
	v_mul_f32_e32 v21, v35, v21
	v_mul_f32_e32 v35, v14, v37
	v_mul_f32_e32 v20, v15, v20
	v_med3_f32 v35, v35, s15, v58
	v_med3_f32 v20, v20, s15, v58
	v_cvt_pk_fp8_f32 v36, v35, v20
	v_mul_f32_e32 v37, v16, v59
	v_mul_f32_e32 v20, v17, v21
	v_med3_f32 v21, v37, s15, v58
	v_med3_f32 v20, v20, s15, v58
	v_cvt_pk_fp8_f32 v36, v21, v20 op_sel:[0,0,1]
	global_store_dword v[18:19], v36, off offset:768
	s_cbranch_scc0 .LBB0_1043
	s_add_i32 s8, s10, 0x400
	v_add_u32_e32 v32, 0x4000, v32
	v_add_u32_e32 v22, 0x4000, v22
	s_cmp_gt_i32 s10, -1
	s_mov_b32 s10, s8
	s_cbranch_scc0 .LBB0_1036
